# P0 ada GEMV: 32 row loads in flight per wave (was 8), same accumulation order
# speedup vs baseline: 1.0033x; 1.0033x over previous
.LBB0_14:
	s_mov_b64 s[100:101], 0xc000
	v_mov_b32_e32 v9, s2
	global_load_dword v50, v[10:11], off
	v_lshl_add_u64 v[10:11], v[10:11], 0, s[100:101]
	global_load_dword v51, v[10:11], off
	v_lshl_add_u64 v[10:11], v[10:11], 0, s[100:101]
	global_load_dword v52, v[10:11], off
	v_lshl_add_u64 v[10:11], v[10:11], 0, s[100:101]
	global_load_dword v53, v[10:11], off
	v_lshl_add_u64 v[10:11], v[10:11], 0, s[100:101]
	global_load_dword v54, v[10:11], off
	v_lshl_add_u64 v[10:11], v[10:11], 0, s[100:101]
	global_load_dword v55, v[10:11], off
	v_lshl_add_u64 v[10:11], v[10:11], 0, s[100:101]
	global_load_dword v56, v[10:11], off
	v_lshl_add_u64 v[10:11], v[10:11], 0, s[100:101]
	global_load_dword v57, v[10:11], off
	v_lshl_add_u64 v[10:11], v[10:11], 0, s[100:101]
	global_load_dword v58, v[10:11], off
	v_lshl_add_u64 v[10:11], v[10:11], 0, s[100:101]
	global_load_dword v59, v[10:11], off
	v_lshl_add_u64 v[10:11], v[10:11], 0, s[100:101]
	global_load_dword v60, v[10:11], off
	v_lshl_add_u64 v[10:11], v[10:11], 0, s[100:101]
	global_load_dword v61, v[10:11], off
	v_lshl_add_u64 v[10:11], v[10:11], 0, s[100:101]
	global_load_dword v62, v[10:11], off
	v_lshl_add_u64 v[10:11], v[10:11], 0, s[100:101]
	global_load_dword v63, v[10:11], off
	v_lshl_add_u64 v[10:11], v[10:11], 0, s[100:101]
	global_load_dword v64, v[10:11], off
	v_lshl_add_u64 v[10:11], v[10:11], 0, s[100:101]
	global_load_dword v65, v[10:11], off
	v_lshl_add_u64 v[10:11], v[10:11], 0, s[100:101]
	global_load_dword v66, v[10:11], off
	v_lshl_add_u64 v[10:11], v[10:11], 0, s[100:101]
	global_load_dword v67, v[10:11], off
	v_lshl_add_u64 v[10:11], v[10:11], 0, s[100:101]
	global_load_dword v68, v[10:11], off
	v_lshl_add_u64 v[10:11], v[10:11], 0, s[100:101]
	global_load_dword v69, v[10:11], off
	v_lshl_add_u64 v[10:11], v[10:11], 0, s[100:101]
	global_load_dword v70, v[10:11], off
	v_lshl_add_u64 v[10:11], v[10:11], 0, s[100:101]
	global_load_dword v71, v[10:11], off
	v_lshl_add_u64 v[10:11], v[10:11], 0, s[100:101]
	global_load_dword v72, v[10:11], off
	v_lshl_add_u64 v[10:11], v[10:11], 0, s[100:101]
	global_load_dword v73, v[10:11], off
	v_lshl_add_u64 v[10:11], v[10:11], 0, s[100:101]
	global_load_dword v74, v[10:11], off
	v_lshl_add_u64 v[10:11], v[10:11], 0, s[100:101]
	global_load_dword v75, v[10:11], off
	v_lshl_add_u64 v[10:11], v[10:11], 0, s[100:101]
	global_load_dword v76, v[10:11], off
	v_lshl_add_u64 v[10:11], v[10:11], 0, s[100:101]
	global_load_dword v77, v[10:11], off
	v_lshl_add_u64 v[10:11], v[10:11], 0, s[100:101]
	global_load_dword v78, v[10:11], off
	v_lshl_add_u64 v[10:11], v[10:11], 0, s[100:101]
	global_load_dword v79, v[10:11], off
	v_lshl_add_u64 v[10:11], v[10:11], 0, s[100:101]
	global_load_dword v80, v[10:11], off
	v_lshl_add_u64 v[10:11], v[10:11], 0, s[100:101]
	global_load_dword v81, v[10:11], off
	v_lshl_add_u64 v[10:11], v[10:11], 0, s[100:101]
	ds_read_b128 v[82:85], v9
	ds_read_b128 v[86:89], v9 offset:16
	ds_read_b128 v[90:93], v9 offset:32
	ds_read_b128 v[94:97], v9 offset:48
	ds_read_b128 v[98:101], v9 offset:64
	ds_read_b128 v[102:105], v9 offset:80
	ds_read_b128 v[106:109], v9 offset:96
	ds_read_b128 v[110:113], v9 offset:112
	ds_read_b128 v[114:117], v9 offset:8192
	ds_read_b128 v[118:121], v9 offset:8208
	ds_read_b128 v[122:125], v9 offset:8224
	ds_read_b128 v[126:129], v9 offset:8240
	ds_read_b128 v[130:133], v9 offset:8256
	ds_read_b128 v[134:137], v9 offset:8272
	ds_read_b128 v[138:141], v9 offset:8288
	ds_read_b128 v[142:145], v9 offset:8304
	s_add_i32 s3, s3, 32
	s_add_i32 s2, s2, 128
	s_cmp_ge_u32 s3, s20
	s_waitcnt lgkmcnt(0)
	s_waitcnt vmcnt(31)
	v_fmac_f32_e32 v12, v50, v82
	v_fmac_f32_e32 v13, v50, v114
	s_waitcnt vmcnt(30)
	v_fmac_f32_e32 v12, v51, v83
	v_fmac_f32_e32 v13, v51, v115
	s_waitcnt vmcnt(29)
	v_fmac_f32_e32 v12, v52, v84
	v_fmac_f32_e32 v13, v52, v116
	s_waitcnt vmcnt(28)
	v_fmac_f32_e32 v12, v53, v85
	v_fmac_f32_e32 v13, v53, v117
	s_waitcnt vmcnt(27)
	v_fmac_f32_e32 v12, v54, v86
	v_fmac_f32_e32 v13, v54, v118
	s_waitcnt vmcnt(26)
	v_fmac_f32_e32 v12, v55, v87
	v_fmac_f32_e32 v13, v55, v119
	s_waitcnt vmcnt(25)
	v_fmac_f32_e32 v12, v56, v88
	v_fmac_f32_e32 v13, v56, v120
	s_waitcnt vmcnt(24)
	v_fmac_f32_e32 v12, v57, v89
	v_fmac_f32_e32 v13, v57, v121
	s_waitcnt vmcnt(23)
	v_fmac_f32_e32 v12, v58, v90
	v_fmac_f32_e32 v13, v58, v122
	s_waitcnt vmcnt(22)
	v_fmac_f32_e32 v12, v59, v91
	v_fmac_f32_e32 v13, v59, v123
	s_waitcnt vmcnt(21)
	v_fmac_f32_e32 v12, v60, v92
	v_fmac_f32_e32 v13, v60, v124
	s_waitcnt vmcnt(20)
	v_fmac_f32_e32 v12, v61, v93
	v_fmac_f32_e32 v13, v61, v125
	s_waitcnt vmcnt(19)
	v_fmac_f32_e32 v12, v62, v94
	v_fmac_f32_e32 v13, v62, v126
	s_waitcnt vmcnt(18)
	v_fmac_f32_e32 v12, v63, v95
	v_fmac_f32_e32 v13, v63, v127
	s_waitcnt vmcnt(17)
	v_fmac_f32_e32 v12, v64, v96
	v_fmac_f32_e32 v13, v64, v128
	s_waitcnt vmcnt(16)
	v_fmac_f32_e32 v12, v65, v97
	v_fmac_f32_e32 v13, v65, v129
	s_waitcnt vmcnt(15)
	v_fmac_f32_e32 v12, v66, v98
	v_fmac_f32_e32 v13, v66, v130
	s_waitcnt vmcnt(14)
	v_fmac_f32_e32 v12, v67, v99
	v_fmac_f32_e32 v13, v67, v131
	s_waitcnt vmcnt(13)
	v_fmac_f32_e32 v12, v68, v100
	v_fmac_f32_e32 v13, v68, v132
	s_waitcnt vmcnt(12)
	v_fmac_f32_e32 v12, v69, v101
	v_fmac_f32_e32 v13, v69, v133
	s_waitcnt vmcnt(11)
	v_fmac_f32_e32 v12, v70, v102
	v_fmac_f32_e32 v13, v70, v134
	s_waitcnt vmcnt(10)
	v_fmac_f32_e32 v12, v71, v103
	v_fmac_f32_e32 v13, v71, v135
	s_waitcnt vmcnt(9)
	v_fmac_f32_e32 v12, v72, v104
	v_fmac_f32_e32 v13, v72, v136
	s_waitcnt vmcnt(8)
	v_fmac_f32_e32 v12, v73, v105
	v_fmac_f32_e32 v13, v73, v137
	s_waitcnt vmcnt(7)
	v_fmac_f32_e32 v12, v74, v106
	v_fmac_f32_e32 v13, v74, v138
	s_waitcnt vmcnt(6)
	v_fmac_f32_e32 v12, v75, v107
	v_fmac_f32_e32 v13, v75, v139
	s_waitcnt vmcnt(5)
	v_fmac_f32_e32 v12, v76, v108
	v_fmac_f32_e32 v13, v76, v140
	s_waitcnt vmcnt(4)
	v_fmac_f32_e32 v12, v77, v109
	v_fmac_f32_e32 v13, v77, v141
	s_waitcnt vmcnt(3)
	v_fmac_f32_e32 v12, v78, v110
	v_fmac_f32_e32 v13, v78, v142
	s_waitcnt vmcnt(2)
	v_fmac_f32_e32 v12, v79, v111
	v_fmac_f32_e32 v13, v79, v143
	s_waitcnt vmcnt(1)
	v_fmac_f32_e32 v12, v80, v112
	v_fmac_f32_e32 v13, v80, v144
	s_waitcnt vmcnt(0)
	v_fmac_f32_e32 v12, v81, v113
	v_fmac_f32_e32 v13, v81, v145
	s_cbranch_scc0 .LBB0_14
	v_add_u32_e32 v9, s21, v1
	s_andn2_b64 vcc, exec, s[8:9]
	ds_write_b64 v9, v[12:13] offset:16384
	s_waitcnt lgkmcnt(0)
	s_barrier
	s_cbranch_vccnz .LBB0_10
	s_load_dwordx16 s[64:79], s[0:1], 0x0
	v_lshl_or_b32 v10, s26, 6, v206
	v_ashrrev_i32_e32 v11, 31, v10
	v_lshlrev_b64 v[28:29], 2, v[10:11]
	v_add_u32_e32 v15, 0, v1
	s_waitcnt lgkmcnt(0)
	v_lshl_add_u64 v[10:11], s[74:75], 0, v[28:29]
	global_load_dword v9, v[10:11], off
	ds_read2st64_b64 v[10:13], v15 offset0:32 offset1:33
	ds_read2st64_b64 v[16:19], v15 offset0:34 offset1:35
	ds_read2st64_b64 v[20:23], v15 offset0:36 offset1:37
	ds_read2st64_b64 v[24:27], v15 offset0:38 offset1:39
	s_load_dwordx16 s[64:79], s[0:1], 0xc0
	s_waitcnt lgkmcnt(0)
	v_add_f32_e32 v10, 0, v10
	v_add_f32_e32 v11, 0, v11
	v_add_f32_e32 v10, v10, v12
	v_add_f32_e32 v11, v11, v13
	v_add_f32_e32 v10, v10, v16
	v_add_f32_e32 v11, v11, v17
	v_add_f32_e32 v10, v10, v18
	v_add_f32_e32 v11, v11, v19
	v_add_f32_e32 v10, v10, v20
	v_add_f32_e32 v11, v11, v21
	v_add_f32_e32 v10, v10, v22
	v_add_f32_e32 v11, v11, v23
	v_add_f32_e32 v10, v10, v24
	v_lshl_add_u64 v[28:29], s[6:7], 0, v[28:29]
	v_add_f32_e32 v11, v11, v25
	v_add_f32_e32 v10, v10, v26
	v_add_co_u32_e32 v30, vcc, 0xc000, v28
	v_add_f32_e32 v11, v11, v27
	s_nop 0
	v_addc_co_u32_e32 v31, vcc, 0, v29, vcc
	s_waitcnt vmcnt(0)
	v_add_f32_e32 v10, v10, v9
	v_add_f32_e32 v9, v11, v9
	global_store_dword v[28:29], v10, off
	global_store_dword v[30:31], v9, off
	s_branch .LBB0_10
